# MoE up/down phases: unit index uses c' = (blockIdx % 8) * (grid / 8) + blockIdx / 8 (any grid that is a multiple of 8; otherwise unchanged) so that each XCD works on whole row blocks
# baseline (speedup 1.0000x reference)
.LBB0_6:
	s_ashr_i32 s3, s2, 31
	s_lshr_b32 s0, s3, 29
	s_add_i32 s5, s2, s0
	s_and_b32 s0, s5, -8
	s_sub_i32 s18, s2, s0
	s_lshl_b32 s0, s18, 4
	s_cmp_lt_i32 s18, 0
	s_mul_i32 s1, s18, 17
	s_cselect_b32 s0, s1, s0
	s_lshl_b32 s1, s18, 7
	s_cmp_lt_i32 s18, 0
	s_mul_i32 s4, s18, 0x81
	s_cselect_b32 s1, s4, s1
	s_lshl_b32 s4, s18, 6
	s_cmp_lt_i32 s18, 0
	s_movk_i32 s6, 0xc1
	s_mul_i32 s7, s18, 0x41
	s_movk_i32 s9, 0x181
	s_cselect_b32 s6, s6, 0xc0
	s_cselect_b32 s9, s9, 0x180
	s_cselect_b32 s4, s7, s4
	s_lshl_b32 s11, s2, 3
	s_lshl_b32 s7, s2, 9
	s_cmp_eq_u32 s8, 15
	v_writelane_b32 v253, s7, 6
	s_cselect_b64 s[12:13], -1, 0
	v_writelane_b32 v253, s12, 7
	s_cmp_eq_u32 s8, 14
	v_mov_b32_e32 v35, 0
	v_writelane_b32 v253, s13, 8
	s_cselect_b64 s[12:13], -1, 0
	v_writelane_b32 v253, s12, 9
	s_cmp_eq_u32 s8, 13
	s_mov_b32 s59, 0x20000
	v_writelane_b32 v253, s13, 10
	s_cselect_b64 s[12:13], -1, 0
	v_writelane_b32 v253, s12, 11
	s_cmp_eq_u32 s8, 12
	v_mbcnt_lo_u32_b32 v1, -1, 0
	v_writelane_b32 v253, s13, 12
	s_cselect_b64 s[12:13], -1, 0
	v_writelane_b32 v253, s12, 13
	s_cmp_eq_u32 s8, 11
	v_mov_b32_e32 v214, 0x358637bd
	v_writelane_b32 v253, s13, 14
	s_cselect_b64 s[12:13], -1, 0
	v_writelane_b32 v253, s12, 15
	s_cmp_eq_u32 s8, 10
	v_mov_b32_e32 v215, 1
	v_writelane_b32 v253, s13, 16
	s_cselect_b64 s[12:13], -1, 0
	v_writelane_b32 v253, s12, 17
	s_cmp_eq_u32 s8, 9
	s_movk_i32 s66, 0x4800
	v_writelane_b32 v253, s13, 18
	s_cselect_b64 s[12:13], -1, 0
	v_writelane_b32 v253, s12, 19
	s_cmp_eq_u32 s8, 8
	s_mov_b32 s67, s59
	v_writelane_b32 v253, s13, 20
	s_cselect_b64 s[12:13], -1, 0
	v_writelane_b32 v253, s12, 21
	s_cmp_eq_u32 s8, 7
	s_mov_b32 s58, 0x4f700000
	v_writelane_b32 v253, s13, 22
	s_cselect_b64 s[12:13], -1, 0
	v_writelane_b32 v253, s12, 23
	s_cmp_eq_u32 s8, 6
	v_mov_b32_e32 v216, 0x3a27c5ac
	v_writelane_b32 v253, s13, 24
	s_cselect_b64 s[12:13], -1, 0
	v_writelane_b32 v253, s12, 25
	s_cmp_eq_u32 s8, 5
	v_mov_b32_e32 v234, v35
	v_writelane_b32 v253, s13, 26
	s_cselect_b64 s[12:13], -1, 0
	v_writelane_b32 v253, s12, 27
	s_cmp_eq_u32 s8, 4
	v_mov_b32_e32 v235, v35
	v_writelane_b32 v253, s13, 28
	s_cselect_b64 s[12:13], -1, 0
	v_writelane_b32 v253, s12, 29
	s_cmp_eq_u32 s8, 3
	v_mov_b32_e32 v236, v35
	v_writelane_b32 v253, s13, 30
	s_cselect_b64 s[12:13], -1, 0
	v_writelane_b32 v253, s12, 31
	s_cmp_eq_u32 s8, 2
	v_mov_b32_e32 v237, v35
	v_writelane_b32 v253, s13, 32
	s_cselect_b64 s[12:13], -1, 0
	v_writelane_b32 v253, s12, 33
	s_cmp_eq_u32 s8, 1
	v_mov_b32_e32 v217, 2
	v_writelane_b32 v253, s13, 34
	s_cselect_b64 s[12:13], -1, 0
	v_writelane_b32 v253, s12, 35
	s_cmp_eq_u32 s8, 0
	v_mbcnt_hi_u32_b32 v218, -1, v1
	v_writelane_b32 v253, s13, 36
	s_cselect_b64 s[12:13], -1, 0
	v_writelane_b32 v253, s12, 37
	s_lshl_b32 s7, s8, 6
	s_cmpk_lt_i32 s2, 0xc00
	v_writelane_b32 v253, s13, 38
	v_writelane_b32 v253, s7, 39
	s_cselect_b64 s[12:13], -1, 0
	s_ashr_i32 s8, s5, 3
	v_writelane_b32 v253, s12, 40
	s_cmpk_lt_i32 s2, 0x600
	s_mul_i32 s5, s6, s18
	v_writelane_b32 v253, s13, 41
	s_cselect_b64 s[12:13], -1, 0
	s_add_i32 s5, s5, s8
	s_mul_hi_i32 s6, s5, 0x2aaaaaab
	s_lshr_b32 s7, s6, 31
	s_ashr_i32 s6, s6, 3
	s_add_i32 s6, s6, s7
	s_mul_i32 s7, s6, 48
	s_sub_i32 s5, s5, s7
	s_bfe_i32 s7, s5, 0x80000
	s_bfe_u32 s7, s7, 0x2000d
	s_add_i32 s7, s5, s7
	s_bfe_i32 s10, s7, 0x80000
	s_and_b32 s7, s7, 0xfc
	s_sub_i32 s5, s5, s7
	s_lshl_b32 s6, s6, 2
	s_sext_i32_i8 s5, s5
	v_writelane_b32 v253, s12, 42
	s_add_i32 s14, s6, s5
	s_mov_b32 s6, s14
	v_writelane_b32 v253, s13, 43
	s_ashr_i32 s15, s14, 31
	v_writelane_b32 v253, s6, 44
	s_sext_i32_i16 s10, s10
	s_ashr_i32 s16, s10, 4
	v_writelane_b32 v253, s7, 45
	s_lshl_b64 s[6:7], s[14:15], 19
	v_writelane_b32 v253, s6, 46
	s_lshl_b32 s5, s16, 9
	s_ashr_i32 s17, s16, 31
	v_writelane_b32 v253, s7, 47
	v_writelane_b32 v253, s5, 48
	s_ashr_i32 s5, s5, 31
	v_writelane_b32 v253, s5, 49
	s_mov_b32 s6, s16
	v_writelane_b32 v253, s6, 50
	s_ashr_i32 s12, s10, 2
	s_lshl_b32 s5, s12, 17
	v_writelane_b32 v253, s7, 51
	s_lshl_b64 s[6:7], s[16:17], 19
	v_writelane_b32 v253, s6, 52
	s_and_b32 s5, s5, 0x60000
	s_cmpk_lt_i32 s2, 0x200
	v_writelane_b32 v253, s7, 53
	v_writelane_b32 v253, s12, 54
	v_writelane_b32 v253, s5, 55
	s_cselect_b64 s[6:7], -1, 0
	v_writelane_b32 v253, s6, 56
	s_cmp_lt_i32 s2, 32
	v_mov_b64_e32 v[200:201], 0xc00
	v_writelane_b32 v253, s7, 57
	s_cselect_b64 s[6:7], -1, 0
	s_cmp_gt_i32 s2, 31
	v_writelane_b32 v253, s6, 58
	s_cselect_b64 s[12:13], -1, 0
	v_mov_b64_e32 v[202:203], 0xbff
	v_writelane_b32 v253, s7, 59
	s_and_b64 s[6:7], s[12:13], exec
	s_cselect_b32 s5, s2, 0x800
	s_bitcmp1_b32 s2, 3
	s_cselect_b64 s[6:7], -1, 0
	v_writelane_b32 v253, s12, 60
	s_and_b64 s[94:95], s[12:13], s[6:7]
	s_cmpk_lt_i32 s11, 0x4000
	v_writelane_b32 v253, s13, 61
	s_cselect_b64 s[6:7], -1, 0
	s_cmpk_lt_u32 s5, 0x800
	v_writelane_b32 v253, s11, 62
	s_cselect_b64 s[10:11], -1, 0
	s_or_b64 s[6:7], s[6:7], s[10:11]
	v_writelane_b32 v253, s5, 63
	v_writelane_b32 v254, s6, 0
	s_mul_i32 s5, s2, 0x120000
	s_lshl_b32 s80, s2, 6
	v_writelane_b32 v254, s7, 1
	s_add_i32 s6, s5, 0x3c800000
	v_writelane_b32 v254, s6, 2
	s_add_i32 s6, s5, 0x3c804800
	v_writelane_b32 v254, s6, 3
	s_add_i32 s6, s5, 0x3c809000
	v_writelane_b32 v254, s6, 4
	s_add_i32 s6, s5, 0x3c80d800
	v_writelane_b32 v254, s6, 5
	s_add_i32 s6, s5, 0x3c812000
	v_writelane_b32 v254, s6, 6
	s_add_i32 s6, s5, 0x3c816800
	v_writelane_b32 v254, s6, 7
	s_add_i32 s6, s5, 0x3c81b000
	v_writelane_b32 v254, s6, 8
	s_add_i32 s6, s5, 0x3c81f800
	v_writelane_b32 v254, s6, 9
	s_add_i32 s6, s5, 0x3c824000
	v_writelane_b32 v254, s6, 10
	s_add_i32 s5, s5, 0x3c828800
	v_writelane_b32 v254, s5, 11
	s_lshl_b32 s5, s2, 21
	s_add_i32 s6, s5, 0x307fc800
	v_writelane_b32 v254, s6, 12
	s_add_i32 s6, s5, 0x307fd800
	v_writelane_b32 v254, s6, 13
	s_add_i32 s6, s5, 0x307fe800
	v_writelane_b32 v254, s6, 14
	s_add_i32 s6, s5, 0x307ff800
	v_writelane_b32 v254, s6, 15
	s_add_i32 s6, s5, 0x30800800
	v_writelane_b32 v254, s6, 16
	s_add_i32 s6, s5, 0x30801800
	v_writelane_b32 v254, s6, 17
	s_add_i32 s6, s5, 0x30802800
	v_writelane_b32 v254, s6, 18
	s_add_i32 s6, s5, 0x30803800
	s_add_i32 s82, s5, 0x307fb800
	v_writelane_b32 v254, s6, 19
	s_add_i32 s5, s5, 0x30804800
	s_ashr_i32 s81, s80, 31
	v_writelane_b32 v254, s5, 20
	s_lshl_b64 s[6:7], s[2:3], 18
	v_writelane_b32 v254, s6, 21
	s_cmpk_lt_i32 s2, 0x400
	s_mul_i32 s5, s18, s9
	v_writelane_b32 v254, s7, 22
	s_cselect_b64 s[6:7], -1, 0
	s_bfe_u32 s19, s2, 0x10003
	v_writelane_b32 v254, s6, 23
	s_cmpk_lt_i32 s2, 0x80
	v_not_b32_e32 v219, 63
	v_writelane_b32 v254, s7, 24
	s_cselect_b64 s[6:7], -1, 0
	v_writelane_b32 v254, s6, 25
	s_cmpk_gt_i32 s2, 0x7f
	v_not_b32_e32 v220, 31
	v_writelane_b32 v254, s7, 26
	s_cselect_b64 s[6:7], -1, 0
	s_cmpk_lt_i32 s2, 0x100
	s_cselect_b64 s[10:11], -1, 0
	s_add_i32 s5, s5, s8
	v_writelane_b32 v254, s10, 27
	s_mul_hi_i32 s9, s5, 0x2aaaaaab
	s_add_i32 s4, s4, s8
	v_writelane_b32 v254, s11, 28
	s_lshr_b32 s10, s9, 31
	s_ashr_i32 s9, s9, 4
	s_add_i32 s10, s9, s10
	s_mul_i32 s9, s10, 0x60
	s_sub_i32 s5, s5, s9
	s_bfe_i32 s9, s5, 0x80000
	s_bfe_u32 s9, s9, 0x2000d
	s_add_i32 s11, s5, s9
	s_and_b32 s9, s11, 0xfc
	s_sub_i32 s5, s5, s9
	s_ashr_i32 s9, s4, 31
	s_lshr_b32 s9, s9, 28
	s_add_i32 s12, s4, s9
	s_and_b32 s9, s12, 0xfff0
	s_sub_i32 s4, s4, s9
	s_bfe_i32 s9, s4, 0x80000
	s_bfe_u32 s9, s9, 0x2000d
	s_add_i32 s13, s4, s9
	s_and_b32 s9, s13, 0xfc
	s_add_i32 s1, s1, s8
	s_sub_i32 s4, s4, s9
	s_ashr_i32 s9, s1, 31
	s_lshr_b32 s9, s9, 27
	s_add_i32 s14, s1, s9
	s_and_b32 s9, s14, 0xffe0
	s_sub_i32 s1, s1, s9
	s_bfe_i32 s9, s1, 0x80000
	s_bfe_u32 s9, s9, 0x2000d
	s_add_i32 s15, s1, s9
	s_and_b32 s9, s15, 0xfc
	s_sub_i32 s16, s1, s9
	s_lshr_b32 s1, s3, 30
	s_add_i32 s1, s2, s1
	s_ashr_i32 s9, s1, 2
	v_writelane_b32 v254, s9, 29
	s_add_i32 s9, 0, 0x20000
	s_lshl_b32 s17, s8, 2
	s_and_b32 s1, s1, -4
	s_add_i32 s17, s9, s17
	v_writelane_b32 v254, s17, 30
	s_add_i32 s9, s9, s1
	v_writelane_b32 v254, s9, 31
	s_ashr_i32 s9, s8, 31
	s_sub_i32 s24, s2, s1
	s_add_i32 s26, s0, s8
	s_lshl_b64 s[0:1], s[8:9], 18
	v_writelane_b32 v254, s0, 32
	s_sext_i32_i8 s5, s5
	s_sext_i32_i8 s4, s4
	v_writelane_b32 v254, s1, 33
	s_bfe_i32 s1, s11, 0x80000
	s_lshl_b32 s0, s10, 2
	s_sext_i32_i16 s1, s1
	s_add_i32 s20, s0, s5
	s_ashr_i32 s0, s1, 2
	v_writelane_b32 v254, s0, 34
	s_lshr_b32 s0, s1, 2
	s_bfe_i64 s[0:1], s[0:1], 0x100000
	s_lshl_b64 s[0:1], s[0:1], 20
	v_writelane_b32 v254, s0, 35
	s_ashr_i32 s25, s24, 31
	s_mov_b32 s8, s19
	v_writelane_b32 v254, s1, 36
	s_ashr_i32 s0, s12, 4
	s_bfe_i32 s1, s13, 0x80000
	s_lshl_b32 s0, s0, 2
	s_sext_i32_i16 s1, s1
	s_add_i32 s22, s0, s4
	s_lshr_b32 s0, s1, 2
	s_ashr_i32 s5, s1, 2
	s_bfe_i64 s[0:1], s[0:1], 0x100000
	s_lshl_b64 s[0:1], s[0:1], 17
	v_writelane_b32 v254, s0, 37
	s_sext_i32_i8 s4, s16
	s_ashr_i32 s19, s18, 31
	v_writelane_b32 v254, s1, 38
	s_ashr_i32 s0, s14, 5
	s_bfe_i32 s1, s15, 0x80000
	s_lshl_b32 s0, s0, 2
	s_sext_i32_i16 s1, s1
	s_add_i32 s88, s0, s4
	s_lshr_b32 s0, s1, 2
	s_ashr_i32 s83, s1, 2
	s_bfe_i64 s[0:1], s[0:1], 0x100000
	s_lshl_b64 s[14:15], s[0:1], 19
	v_writelane_b32 v254, s14, 39
	s_lshl_b64 s[0:1], s[0:1], 20
	s_ashr_i32 s21, s20, 31
	v_writelane_b32 v254, s15, 40
	v_writelane_b32 v254, s0, 41
	s_ashr_i32 s23, s22, 31
	s_ashr_i32 s89, s88, 31
	v_writelane_b32 v254, s1, 42
	v_writelane_b32 v254, s5, 43
	s_lshl_b32 s0, s5, 9
	v_writelane_b32 v254, s0, 44
	s_ashr_i32 s0, s0, 31
	v_writelane_b32 v254, s0, 45
	s_mov_b32 s0, s24
	v_writelane_b32 v254, s0, 46
	s_ashr_i32 s27, s26, 31
	v_mov_b32_e32 v221, 0x7fc00000
	v_writelane_b32 v254, s1, 47
	s_lshl_b64 s[0:1], s[24:25], 20
	v_writelane_b32 v254, s0, 48
	v_mov_b32_e32 v222, 0x80
	v_mov_b32_e32 v223, 0xff800000
	v_writelane_b32 v254, s1, 49
	s_mov_b32 s0, s18
	v_writelane_b32 v254, s0, 50
	v_mov_b64_e32 v[204:205], 0x400
	v_mov_b64_e32 v[206:207], 0x3ff
	v_writelane_b32 v254, s1, 51
	s_lshl_b64 s[0:1], s[18:19], 18
	v_writelane_b32 v254, s0, 52
	v_mov_b64_e32 v[210:211], 0x7f
	s_movk_i32 s33, 0xc0
	v_writelane_b32 v254, s1, 53
	s_lshr_b32 s97, s93, 3
	s_and_b32 s96, s2, 7
	s_mul_i32 s96, s96, s97
	s_lshr_b32 s97, s2, 3
	s_add_i32 s96, s96, s97
	s_and_b32 s97, s93, 7
	s_cmp_eq_u32 s97, 0
	s_cselect_b32 s96, s96, s2
	v_writelane_b32 v252, s96, 47
	s_lshr_b32 s97, s96, 2
	v_writelane_b32 v254, s97, 29
	s_and_b32 s97, s96, -4
	s_add_i32 s97, s97, 0x20000
	v_writelane_b32 v254, s97, 31
	s_and_b32 s97, s96, 3
	v_writelane_b32 v254, s97, 46
	s_lshl_b32 s97, s97, 20
	v_writelane_b32 v254, s97, 48
	s_lshr_b32 s97, s96, 3
	s_lshl_b32 s97, s97, 2
	s_add_i32 s97, s97, 0x20000
	v_writelane_b32 v254, s97, 30
	s_lshr_b32 s97, s96, 3
	s_lshl_b32 s97, s97, 18
	v_writelane_b32 v254, s97, 32
	s_and_b32 s97, s96, 7
	v_writelane_b32 v254, s97, 50
	s_lshl_b32 s97, s97, 18
	v_writelane_b32 v254, s97, 52
	s_mov_b32 s97, 0
	v_writelane_b32 v254, s97, 47
	v_writelane_b32 v254, s97, 49
	v_writelane_b32 v254, s97, 51
	v_writelane_b32 v254, s97, 53
	v_writelane_b32 v254, s97, 33
	s_mov_b32 s0, s20
	v_writelane_b32 v254, s0, 54
	s_movk_i32 s72, 0x7fff
	s_movk_i32 s73, 0x1000
	v_writelane_b32 v254, s1, 55
	s_lshl_b64 s[0:1], s[20:21], 20
	v_writelane_b32 v254, s0, 56
	s_movk_i32 s90, 0x2000
	s_movk_i32 s91, 0x3000
	v_writelane_b32 v254, s1, 57
	s_mov_b32 s0, s22
	v_writelane_b32 v254, s0, 58
	s_mov_b32 s92, 0x34800000
	s_mov_b32 s97, 0
	v_writelane_b32 v254, s1, 59
	s_lshl_b64 s[0:1], s[22:23], 19
	v_writelane_b32 v254, s0, 60
	s_mov_b64 s[78:79], 0x80
	s_mov_b64 s[76:77], 0x8000000
	v_writelane_b32 v254, s1, 61
	s_lshl_b64 s[0:1], s[88:89], 19
	v_writelane_b32 v254, s0, 62
	s_nop 1
	v_writelane_b32 v254, s1, 63
	s_lshl_b64 s[0:1], s[88:89], 20
	v_writelane_b32 v252, s0, 0
	s_nop 1
	v_writelane_b32 v252, s1, 1
	s_mov_b32 s0, s26
	v_writelane_b32 v252, s0, 2
	s_nop 1
	v_writelane_b32 v252, s1, 3
	s_lshl_b64 s[0:1], s[26:27], 20
	v_writelane_b32 v252, s0, 4
	s_nop 1
	v_writelane_b32 v252, s1, 5
	s_xor_b64 s[0:1], s[94:95], -1
	v_writelane_b32 v252, s0, 6
	s_nop 1
	v_writelane_b32 v252, s1, 7
	s_add_u32 s0, s60, 0x1000
	v_writelane_b32 v252, s0, 8
	s_addc_u32 s0, s61, 0
	v_writelane_b32 v252, s0, 9
	s_xor_b64 s[0:1], s[6:7], -1
	v_writelane_b32 v252, s0, 10
	s_add_i32 s4, 0, 0x20600
	s_mov_b32 s6, 0x3ffff
	v_writelane_b32 v252, s1, 11
	s_lshl_b32 s0, s2, 4
	v_writelane_b32 v252, s0, 12
	s_lshl_b32 s0, s2, 7
	v_writelane_b32 v252, s0, 13
	s_or_b32 s0, s0, 1
	v_writelane_b32 v252, s0, 14
	s_lshl_b32 s0, s2, 5
	v_writelane_b32 v252, s0, 15
	s_lshl_b32 s0, s2, 8
	v_writelane_b32 v252, s0, 16
	s_add_i32 s0, 0, 0x24020
	v_writelane_b32 v252, s0, 17
	s_add_i32 s0, 0, 0x24024
	v_writelane_b32 v252, s0, 18
	v_writelane_b32 v252, s4, 19
	s_add_i32 s4, 0, 0x20800
	v_writelane_b32 v252, s4, 20
	s_add_i32 s4, 0, 0x20a00
	v_writelane_b32 v252, s4, 21
	s_lshl_b64 s[4:5], s[80:81], 2
	v_writelane_b32 v252, s4, 22
	s_mov_b32 s0, 0x24800000
	s_mov_b32 s1, 0x2c800000
	v_writelane_b32 v252, s5, 23
	s_load_dwordx2 s[4:5], s[84:85], 0x100
	v_writelane_b32 v252, s84, 24
	s_waitcnt lgkmcnt(0)
	s_mov_b32 s48, s4
	v_writelane_b32 v252, s85, 25
	v_writelane_b32 v252, s93, 26
	v_writelane_b32 v252, s86, 27
	s_nop 1
	v_writelane_b32 v252, s87, 28
	v_writelane_b32 v252, s80, 29
	s_nop 1
	v_writelane_b32 v252, s81, 30
	v_writelane_b32 v252, s82, 31
	v_writelane_b32 v252, s88, 32
	s_nop 1
	v_writelane_b32 v252, s89, 33
	v_writelane_b32 v252, s83, 34
	s_branch .LBB0_8
